# speedup vs baseline: 1.0014x; 1.0014x over previous
.LBB1_9:
	s_or_b64 exec, exec, s[2:3]
	s_waitcnt vmcnt(6)
	v_cndmask_b32_e64 v64, 0, 1, s[8:9]
	v_cmp_ne_u32_e64 s[2:3], 1, v64
	s_andn2_b64 vcc, exec, s[8:9]
	s_waitcnt lgkmcnt(0)
	s_barrier
	s_cbranch_vccnz .LBB1_18
	s_mov_b64 s[16:17], -1
	s_and_b64 vcc, exec, s[10:11]
	s_cbranch_vccz .LBB1_12
	s_setprio 0
	s_mov_b64 s[16:17], 0

.LBB1_20:
	s_or_b64 exec, exec, s[20:21]
	s_and_b64 vcc, exec, s[2:3]
	s_waitcnt lgkmcnt(0)
	s_barrier
	s_cbranch_vccnz .LBB1_29
	s_mov_b64 s[2:3], -1
	s_and_b64 vcc, exec, s[10:11]
	s_cbranch_vccz .LBB1_23
	s_setprio 0
	s_mov_b64 s[2:3], 0
